# speedup vs baseline: 1.0123x; 1.0006x over previous
.LBB3_11:
	v_and_b32_e32 v133, 64, v222
	v_xor_b32_e32 v132, 16, v222
	v_add_u32_e32 v133, 64, v133
	v_cmp_lt_i32_e64 s[2:3], v132, v133
	v_exp_f32_e32 v134, v114
	v_exp_f32_e32 v136, v116
	v_cndmask_b32_e64 v132, v222, v132, s[2:3]
	v_lshlrev_b32_e32 v140, 2, v132
	v_xor_b32_e32 v132, 32, v222
	v_exp_f32_e32 v137, v117
	v_exp_f32_e32 v135, v115
	v_cmp_lt_i32_e64 s[2:3], v132, v133
	v_or_b32_e32 v130, s42, v209
	v_or_b32_e32 v131, s41, v210
	v_cndmask_b32_e64 v132, v222, v132, s[2:3]
	s_lshr_b32 s2, s41, 7
	v_add_u32_e32 v194, s2, v206
	v_lshlrev_b32_e32 v141, 7, v130
	v_lshlrev_b32_e32 v139, 2, v132
	v_lshlrev_b64 v[132:133], 14, v[194:195]
	v_and_b32_e32 v194, 0x7b700, v141
	v_add_u32_e32 v142, 0x400, v131
	v_pk_add_f32 v[136:137], v[136:137], 1.0 op_sel_hi:[1,0]
	v_pk_add_f32 v[144:145], v[134:135], 1.0 op_sel_hi:[1,0]
	v_lshl_add_u64 v[146:147], v[200:201], 0, v[194:195]
	v_lshrrev_b32_e32 v194, 6, v142
	v_rcp_f32_e64 v143, -v137
	v_rcp_f32_e64 v142, -v136
	v_rcp_f32_e64 v149, -v145
	v_rcp_f32_e64 v148, -v144
	v_exp_f32_e32 v154, v80
	v_pk_fma_f32 v[152:153], v[142:143], 2.0, 1.0 op_sel_hi:[1,0,0]
	v_exp_f32_e32 v155, v81
	v_pk_fma_f32 v[142:143], v[148:149], 2.0, 1.0 op_sel_hi:[1,0,0]
	v_exp_f32_e32 v148, v78
	v_exp_f32_e32 v149, v79
	v_pk_add_f32 v[154:155], v[154:155], 1.0 op_sel_hi:[1,0]
	v_cvt_pk_bf16_f32 v142, v142, v143
	v_rcp_f32_e64 v157, -v155
	v_pk_add_f32 v[148:149], v[148:149], 1.0 op_sel_hi:[1,0]
	v_rcp_f32_e64 v156, -v154
	v_rcp_f32_e64 v159, -v149
	v_rcp_f32_e64 v158, -v148
	v_cvt_pk_bf16_f32 v143, v152, v153
	v_pk_fma_f32 v[152:153], v[156:157], 2.0, 1.0 op_sel_hi:[1,0,0]
	v_pk_mul_f32 v[148:149], v[144:145], v[148:149]
	v_pk_fma_f32 v[156:157], v[158:159], 2.0, 1.0 op_sel_hi:[1,0,0]
	v_cvt_pk_bf16_f32 v145, v152, v153
	v_cvt_pk_bf16_f32 v144, v156, v157
	v_exp_f32_e32 v152, v106
	v_exp_f32_e32 v153, v107
	v_exp_f32_e32 v156, v108
	v_exp_f32_e32 v157, v109
	v_pk_mul_f32 v[136:137], v[136:137], v[154:155]
	v_pk_add_f32 v[152:153], v[152:153], 1.0 op_sel_hi:[1,0]
	v_pk_add_f32 v[116:117], v[116:117], 0 op_sel_hi:[1,0]
	v_pk_add_f32 v[156:157], v[156:157], 1.0 op_sel_hi:[1,0]
	v_rcp_f32_e64 v163, -v153
	v_rcp_f32_e64 v161, -v157
	v_rcp_f32_e64 v160, -v156
	v_rcp_f32_e64 v162, -v152
	v_pk_mul_f32 v[148:149], v[148:149], v[152:153]
	v_pk_mul_f32 v[136:137], v[136:137], v[156:157]
	v_exp_f32_e32 v152, v70
	v_exp_f32_e32 v156, v72
	v_exp_f32_e32 v157, v73
	v_exp_f32_e32 v153, v71
	v_pk_add_f32 v[114:115], v[114:115], 0 op_sel_hi:[1,0]
	v_pk_add_f32 v[154:155], v[116:117], v[80:81]
	v_pk_add_f32 v[158:159], v[114:115], v[78:79]
	v_pk_add_f32 v[108:109], v[154:155], v[108:109]
	v_pk_add_f32 v[154:155], v[156:157], 1.0 op_sel_hi:[1,0]
	v_pk_add_f32 v[152:153], v[152:153], 1.0 op_sel_hi:[1,0]
	v_lshlrev_b64 v[134:135], 19, v[194:195]
	v_pk_add_f32 v[106:107], v[158:159], v[106:107]
	v_rcp_f32_e64 v157, -v155
	v_rcp_f32_e64 v156, -v154
	v_rcp_f32_e64 v159, -v153
	v_rcp_f32_e64 v158, -v152
	v_lshl_add_u64 v[150:151], v[146:147], 0, v[134:135]
	v_lshlrev_b32_e32 v194, 1, v198
	v_add_u32_e32 v138, s43, v207
	v_permlane16_swap_b32_e32 v142, v144
	v_permlane16_swap_b32_e32 v143, v145
	v_lshl_add_u64 v[150:151], v[150:151], 0, v[194:195]
	ds_read_b128 v[114:117], v138
	ds_read_b128 v[78:81], v138 offset:64
	global_store_dwordx4 v[150:151], v[142:145], off nt
	s_bitcmp1_b32 s20, 12
	s_cbranch_scc1 .Lg1_noX
	s_barrier
.Lg1_noX:
	v_pk_fma_f32 v[156:157], v[156:157], 2.0, 1.0 op_sel_hi:[1,0,0]
	v_pk_mul_f32 v[154:155], v[136:137], v[154:155]
	v_pk_fma_f32 v[144:145], v[160:161], 2.0, 1.0 op_sel_hi:[1,0,0]
	v_pk_fma_f32 v[142:143], v[162:163], 2.0, 1.0 op_sel_hi:[1,0,0]
	v_pk_mul_f32 v[148:149], v[148:149], v[152:153]
	v_cvt_pk_bf16_f32 v142, v142, v143
	v_cvt_pk_bf16_f32 v143, v144, v145
	v_pk_fma_f32 v[144:145], v[158:159], 2.0, 1.0 op_sel_hi:[1,0,0]
	v_pk_add_f32 v[152:153], v[108:109], v[72:73]
	v_cvt_pk_bf16_f32 v144, v144, v145
	v_cvt_pk_bf16_f32 v145, v156, v157
	s_nop 0
	v_permlane16_swap_b32_e32 v142, v144
	v_permlane16_swap_b32_e32 v143, v145
	v_pk_add_f32 v[158:159], v[106:107], v[70:71]
	ds_read_b128 v[106:109], v138 offset:128
	ds_read_b128 v[70:73], v138 offset:192
	global_store_dwordx4 v[150:151], v[142:145], off offset:128 nt
	v_exp_f32_e32 v136, v90
	v_exp_f32_e32 v137, v91
	v_exp_f32_e32 v142, v92
	v_exp_f32_e32 v143, v93
	v_add_u32_e32 v131, 0x480, v131
	v_pk_add_f32 v[150:151], v[136:137], 1.0 op_sel_hi:[1,0]
	v_ashrrev_i32_e32 v144, 6, v131
	v_pk_add_f32 v[142:143], v[142:143], 1.0 op_sel_hi:[1,0]
	v_rcp_f32_e64 v161, -v151
	v_rcp_f32_e64 v157, -v143
	v_rcp_f32_e64 v156, -v142
	v_rcp_f32_e64 v160, -v150
	v_pk_mul_f32 v[148:149], v[148:149], v[150:151]
	v_pk_mul_f32 v[150:151], v[154:155], v[142:143]
	v_exp_f32_e32 v142, v42
	v_exp_f32_e32 v154, v44
	v_exp_f32_e32 v155, v45
	v_exp_f32_e32 v143, v43
	v_ashrrev_i32_e32 v145, 31, v144
	v_pk_add_f32 v[92:93], v[152:153], v[92:93]
	v_pk_add_f32 v[152:153], v[154:155], 1.0 op_sel_hi:[1,0]
	v_pk_add_f32 v[154:155], v[142:143], 1.0 op_sel_hi:[1,0]
	v_lshlrev_b64 v[136:137], 19, v[144:145]
	v_pk_fma_f32 v[144:145], v[156:157], 2.0, 1.0 op_sel_hi:[1,0,0]
	v_pk_fma_f32 v[156:157], v[160:161], 2.0, 1.0 op_sel_hi:[1,0,0]
	v_pk_add_f32 v[90:91], v[158:159], v[90:91]
	v_rcp_f32_e64 v159, -v153
	v_rcp_f32_e64 v158, -v152
	v_rcp_f32_e64 v161, -v155
	v_rcp_f32_e64 v160, -v154
	v_cvt_pk_bf16_f32 v142, v156, v157
	v_cvt_pk_bf16_f32 v143, v144, v145
	v_pk_fma_f32 v[156:157], v[158:159], 2.0, 1.0 op_sel_hi:[1,0,0]
	v_pk_fma_f32 v[144:145], v[160:161], 2.0, 1.0 op_sel_hi:[1,0,0]
	v_exp_f32_e32 v158, v128
	v_cvt_pk_bf16_f32 v144, v144, v145
	v_cvt_pk_bf16_f32 v145, v156, v157
	v_exp_f32_e32 v156, v126
	v_exp_f32_e32 v159, v129
	v_exp_f32_e32 v157, v127
	v_lshl_add_u64 v[146:147], v[146:147], 0, v[136:137]
	v_pk_mul_f32 v[150:151], v[150:151], v[152:153]
	v_pk_mul_f32 v[148:149], v[148:149], v[154:155]
	v_pk_add_f32 v[158:159], v[158:159], 1.0 op_sel_hi:[1,0]
	v_pk_add_f32 v[156:157], v[156:157], 1.0 op_sel_hi:[1,0]
	v_lshl_add_u64 v[164:165], v[146:147], 0, v[194:195]
	v_rcp_f32_e64 v163, -v157
	v_rcp_f32_e64 v162, -v156
	v_pk_mul_f32 v[146:147], v[148:149], v[156:157]
	v_pk_mul_f32 v[148:149], v[150:151], v[158:159]
	v_exp_f32_e32 v150, v58
	v_exp_f32_e32 v156, v60
	v_exp_f32_e32 v157, v61
	v_exp_f32_e32 v151, v59
	v_pk_add_f32 v[152:153], v[92:93], v[44:45]
	v_pk_add_f32 v[154:155], v[90:91], v[42:43]
	v_pk_add_f32 v[128:129], v[152:153], v[128:129]
	v_pk_add_f32 v[152:153], v[156:157], 1.0 op_sel_hi:[1,0]
	v_pk_add_f32 v[150:151], v[150:151], 1.0 op_sel_hi:[1,0]
	v_pk_mul_f32 v[148:149], v[148:149], v[152:153]
	v_pk_mul_f32 v[146:147], v[146:147], v[150:151]
	v_pk_add_f32 v[126:127], v[154:155], v[126:127]
	v_log_f32_e32 v131, v146
	v_log_f32_e32 v146, v147
	v_log_f32_e32 v147, v148
	v_log_f32_e32 v148, v149
	v_pk_add_f32 v[60:61], v[128:129], v[60:61]
	v_pk_add_f32 v[58:59], v[126:127], v[58:59]
	v_add_f32_e32 v126, v131, v146
	v_add_f32_e32 v127, v147, v148
	v_add_f32_e32 v58, v58, v59
	v_add_f32_e32 v59, v60, v61
	v_add_f32_e32 v126, v126, v127
	v_add_f32_e32 v58, v58, v59
	v_add_f32_e32 v126, 0xc2000000, v126
	v_mul_f32_e32 v131, 0xbeb17218, v58
	v_fmac_f32_e32 v131, 0x3f317218, v126
	v_rcp_f32_e64 v161, -v159
	v_rcp_f32_e64 v160, -v158
	ds_bpermute_b32 v148, v140, v131
	v_rcp_f32_e64 v155, -v153
	v_rcp_f32_e64 v154, -v152
	v_permlane16_swap_b32_e32 v142, v144
	v_permlane16_swap_b32_e32 v143, v145
	ds_read_b128 v[90:93], v138 offset:512
	ds_read_b128 v[42:45], v138 offset:576
	global_store_dwordx4 v[164:165], v[142:145], off nt
	v_rcp_f32_e64 v157, -v151
	v_rcp_f32_e64 v156, -v150
	v_pk_fma_f32 v[142:143], v[160:161], 2.0, 1.0 op_sel_hi:[1,0,0]
	v_pk_fma_f32 v[144:145], v[162:163], 2.0, 1.0 op_sel_hi:[1,0,0]
	s_waitcnt lgkmcnt(0)
	v_add_f32_e32 v131, v131, v148
	v_cvt_pk_bf16_f32 v144, v144, v145
	v_cvt_pk_bf16_f32 v145, v142, v143
	v_pk_fma_f32 v[142:143], v[154:155], 2.0, 1.0 op_sel_hi:[1,0,0]
	ds_read_b128 v[126:129], v138 offset:640
	ds_read_b128 v[58:61], v138 offset:704
	v_cvt_pk_bf16_f32 v147, v142, v143
	ds_bpermute_b32 v142, v139, v131
	v_pk_fma_f32 v[154:155], v[156:157], 2.0, 1.0 op_sel_hi:[1,0,0]
	v_lshl_add_u64 v[132:133], s[14:15], 0, v[132:133]
	v_cvt_pk_bf16_f32 v146, v154, v155
	s_nop 1
	v_permlane16_swap_b32_e32 v144, v146
	v_permlane16_swap_b32_e32 v145, v147
	global_store_dwordx4 v[164:165], v[144:147], off offset:128 nt
	s_and_saveexec_b64 s[2:3], s[0:1]
	s_cbranch_execz .LBB3_13
	s_waitcnt lgkmcnt(0)
	v_add_f32_e32 v144, v131, v142
	v_mov_b32_e32 v131, v195
	v_lshl_add_u64 v[142:143], v[130:131], 2, v[132:133]
	global_store_dword v[142:143], v144, off
.LBB3_13:
	s_or_b64 exec, exec, s[2:3]
	s_waitcnt lgkmcnt(0)
	v_exp_f32_e32 v142, v110
	v_exp_f32_e32 v144, v112
	v_exp_f32_e32 v145, v113
	v_exp_f32_e32 v143, v111
	v_exp_f32_e32 v156, v76
	v_exp_f32_e32 v157, v77
	v_pk_add_f32 v[144:145], v[144:145], 1.0 op_sel_hi:[1,0]
	v_pk_add_f32 v[148:149], v[142:143], 1.0 op_sel_hi:[1,0]
	v_rcp_f32_e64 v143, -v145
	v_rcp_f32_e64 v142, -v144
	v_rcp_f32_e64 v151, -v149
	v_rcp_f32_e64 v150, -v148
	v_pk_add_f32 v[156:157], v[156:157], 1.0 op_sel_hi:[1,0]
	v_pk_fma_f32 v[154:155], v[142:143], 2.0, 1.0 op_sel_hi:[1,0,0]
	v_rcp_f32_e64 v159, -v157
	v_pk_fma_f32 v[142:143], v[150:151], 2.0, 1.0 op_sel_hi:[1,0,0]
	v_exp_f32_e32 v150, v74
	v_exp_f32_e32 v151, v75
	v_rcp_f32_e64 v158, -v156
	v_cvt_pk_bf16_f32 v142, v142, v143
	v_cvt_pk_bf16_f32 v143, v154, v155
	v_pk_add_f32 v[150:151], v[150:151], 1.0 op_sel_hi:[1,0]
	v_pk_fma_f32 v[154:155], v[158:159], 2.0, 1.0 op_sel_hi:[1,0,0]
	v_rcp_f32_e64 v161, -v151
	v_rcp_f32_e64 v160, -v150
	v_pk_mul_f32 v[156:157], v[144:145], v[156:157]
	v_cvt_pk_bf16_f32 v145, v154, v155
	v_exp_f32_e32 v154, v102
	v_pk_fma_f32 v[158:159], v[160:161], 2.0, 1.0 op_sel_hi:[1,0,0]
	v_exp_f32_e32 v155, v103
	v_cvt_pk_bf16_f32 v144, v158, v159
	v_exp_f32_e32 v158, v104
	v_exp_f32_e32 v159, v105
	v_pk_mul_f32 v[148:149], v[148:149], v[150:151]
	v_pk_add_f32 v[154:155], v[154:155], 1.0 op_sel_hi:[1,0]
	v_pk_add_f32 v[112:113], v[112:113], 0 op_sel_hi:[1,0]
	v_pk_add_f32 v[158:159], v[158:159], 1.0 op_sel_hi:[1,0]
	v_rcp_f32_e64 v165, -v155
	v_rcp_f32_e64 v163, -v159
	v_rcp_f32_e64 v162, -v158
	v_rcp_f32_e64 v164, -v154
	v_pk_mul_f32 v[148:149], v[148:149], v[154:155]
	v_pk_mul_f32 v[154:155], v[156:157], v[158:159]
	v_exp_f32_e32 v156, v66
	v_exp_f32_e32 v158, v68
	v_exp_f32_e32 v159, v69
	v_exp_f32_e32 v157, v67
	v_pk_add_f32 v[110:111], v[110:111], 0 op_sel_hi:[1,0]
	v_pk_add_f32 v[150:151], v[112:113], v[76:77]
	v_bitop3_b32 v146, v141, s38, v223 bitop3:0xc8
	v_mov_b32_e32 v147, v195
	v_pk_add_f32 v[160:161], v[110:111], v[74:75]
	v_pk_add_f32 v[104:105], v[150:151], v[104:105]
	v_pk_add_f32 v[150:151], v[158:159], 1.0 op_sel_hi:[1,0]
	v_pk_add_f32 v[156:157], v[156:157], 1.0 op_sel_hi:[1,0]
	v_lshl_add_u64 v[146:147], v[200:201], 0, v[146:147]
	v_pk_add_f32 v[102:103], v[160:161], v[102:103]
	v_rcp_f32_e64 v159, -v151
	v_rcp_f32_e64 v158, -v150
	v_rcp_f32_e64 v161, -v157
	v_rcp_f32_e64 v160, -v156
	v_lshl_add_u64 v[152:153], v[146:147], 0, v[134:135]
	v_permlane16_swap_b32_e32 v142, v144
	v_permlane16_swap_b32_e32 v143, v145
	v_lshl_add_u64 v[152:153], v[152:153], 0, v[194:195]
	ds_read_b128 v[110:113], v138
	ds_read_b128 v[74:77], v138 offset:64
	global_store_dwordx4 v[152:153], v[142:145], off nt
	v_pk_fma_f32 v[158:159], v[158:159], 2.0, 1.0 op_sel_hi:[1,0,0]
	v_pk_mul_f32 v[148:149], v[148:149], v[156:157]
	v_pk_fma_f32 v[144:145], v[162:163], 2.0, 1.0 op_sel_hi:[1,0,0]
	v_pk_fma_f32 v[142:143], v[164:165], 2.0, 1.0 op_sel_hi:[1,0,0]
	v_pk_mul_f32 v[150:151], v[154:155], v[150:151]
	v_cvt_pk_bf16_f32 v142, v142, v143
	v_cvt_pk_bf16_f32 v143, v144, v145
	v_pk_fma_f32 v[144:145], v[160:161], 2.0, 1.0 op_sel_hi:[1,0,0]
	v_exp_f32_e32 v160, v88
	v_cvt_pk_bf16_f32 v144, v144, v145
	v_cvt_pk_bf16_f32 v145, v158, v159
	v_exp_f32_e32 v158, v86
	v_exp_f32_e32 v159, v87
	v_permlane16_swap_b32_e32 v142, v144
	v_exp_f32_e32 v161, v89
	v_permlane16_swap_b32_e32 v143, v145
	v_pk_add_f32 v[158:159], v[158:159], 1.0 op_sel_hi:[1,0]
	v_pk_add_f32 v[154:155], v[104:105], v[68:69]
	v_pk_add_f32 v[156:157], v[102:103], v[66:67]
	ds_read_b128 v[102:105], v138 offset:128
	ds_read_b128 v[66:69], v138 offset:192
	v_rcp_f32_e64 v165, -v159
	v_rcp_f32_e64 v164, -v158
	global_store_dwordx4 v[152:153], v[142:145], off offset:128 nt
	v_pk_mul_f32 v[148:149], v[148:149], v[158:159]
	v_exp_f32_e32 v152, v38
	v_exp_f32_e32 v158, v40
	v_exp_f32_e32 v159, v41
	v_exp_f32_e32 v153, v39
	v_pk_add_f32 v[160:161], v[160:161], 1.0 op_sel_hi:[1,0]
	v_pk_add_f32 v[88:89], v[154:155], v[88:89]
	v_rcp_f32_e64 v163, -v161
	v_rcp_f32_e64 v162, -v160
	v_pk_add_f32 v[154:155], v[158:159], 1.0 op_sel_hi:[1,0]
	v_pk_add_f32 v[152:153], v[152:153], 1.0 op_sel_hi:[1,0]
	v_pk_add_f32 v[86:87], v[156:157], v[86:87]
	v_rcp_f32_e64 v157, -v155
	v_rcp_f32_e64 v156, -v154
	v_rcp_f32_e64 v159, -v153
	v_rcp_f32_e64 v158, -v152
	v_pk_fma_f32 v[144:145], v[162:163], 2.0, 1.0 op_sel_hi:[1,0,0]
	v_pk_fma_f32 v[142:143], v[164:165], 2.0, 1.0 op_sel_hi:[1,0,0]
	v_pk_fma_f32 v[156:157], v[156:157], 2.0, 1.0 op_sel_hi:[1,0,0]
	v_cvt_pk_bf16_f32 v142, v142, v143
	v_cvt_pk_bf16_f32 v143, v144, v145
	v_pk_fma_f32 v[144:145], v[158:159], 2.0, 1.0 op_sel_hi:[1,0,0]
	v_exp_f32_e32 v158, v124
	v_cvt_pk_bf16_f32 v144, v144, v145
	v_cvt_pk_bf16_f32 v145, v156, v157
	v_exp_f32_e32 v156, v122
	v_exp_f32_e32 v159, v125
	v_exp_f32_e32 v157, v123
	v_pk_mul_f32 v[150:151], v[150:151], v[160:161]
	v_lshl_add_u64 v[146:147], v[146:147], 0, v[136:137]
	v_pk_mul_f32 v[150:151], v[150:151], v[154:155]
	v_pk_mul_f32 v[148:149], v[148:149], v[152:153]
	v_pk_add_f32 v[158:159], v[158:159], 1.0 op_sel_hi:[1,0]
	v_pk_add_f32 v[156:157], v[156:157], 1.0 op_sel_hi:[1,0]
	v_lshl_add_u64 v[164:165], v[146:147], 0, v[194:195]
	v_rcp_f32_e64 v163, -v157
	v_rcp_f32_e64 v162, -v156
	v_pk_mul_f32 v[146:147], v[148:149], v[156:157]
	v_pk_mul_f32 v[148:149], v[150:151], v[158:159]
	v_exp_f32_e32 v150, v50
	v_exp_f32_e32 v156, v52
	v_exp_f32_e32 v157, v53
	v_exp_f32_e32 v151, v51
	v_pk_add_f32 v[152:153], v[88:89], v[40:41]
	v_pk_add_f32 v[154:155], v[86:87], v[38:39]
	v_pk_add_f32 v[124:125], v[152:153], v[124:125]
	v_pk_add_f32 v[152:153], v[156:157], 1.0 op_sel_hi:[1,0]
	v_pk_add_f32 v[150:151], v[150:151], 1.0 op_sel_hi:[1,0]
	v_pk_mul_f32 v[148:149], v[148:149], v[152:153]
	v_pk_mul_f32 v[146:147], v[146:147], v[150:151]
	v_pk_add_f32 v[122:123], v[154:155], v[122:123]
	v_log_f32_e32 v131, v146
	v_log_f32_e32 v146, v147
	v_log_f32_e32 v147, v148
	v_log_f32_e32 v148, v149
	v_pk_add_f32 v[52:53], v[124:125], v[52:53]
	v_pk_add_f32 v[50:51], v[122:123], v[50:51]
	v_add_f32_e32 v122, v131, v146
	v_add_f32_e32 v123, v147, v148
	v_add_f32_e32 v50, v50, v51
	v_add_f32_e32 v51, v52, v53
	v_add_f32_e32 v122, v122, v123
	v_add_f32_e32 v50, v50, v51
	v_add_f32_e32 v122, 0xc2000000, v122
	v_mul_f32_e32 v131, 0xbeb17218, v50
	v_fmac_f32_e32 v131, 0x3f317218, v122
	v_rcp_f32_e64 v161, -v159
	v_rcp_f32_e64 v160, -v158
	ds_bpermute_b32 v148, v140, v131
	v_rcp_f32_e64 v155, -v153
	v_rcp_f32_e64 v154, -v152
	v_permlane16_swap_b32_e32 v142, v144
	v_permlane16_swap_b32_e32 v143, v145
	ds_read_b128 v[86:89], v138 offset:512
	ds_read_b128 v[38:41], v138 offset:576
	global_store_dwordx4 v[164:165], v[142:145], off nt
	v_rcp_f32_e64 v157, -v151
	v_rcp_f32_e64 v156, -v150
	v_pk_fma_f32 v[142:143], v[160:161], 2.0, 1.0 op_sel_hi:[1,0,0]
	v_pk_fma_f32 v[144:145], v[162:163], 2.0, 1.0 op_sel_hi:[1,0,0]
	s_waitcnt lgkmcnt(0)
	v_add_f32_e32 v131, v131, v148
	v_cvt_pk_bf16_f32 v144, v144, v145
	v_cvt_pk_bf16_f32 v145, v142, v143
	v_pk_fma_f32 v[142:143], v[154:155], 2.0, 1.0 op_sel_hi:[1,0,0]
	ds_read_b128 v[122:125], v138 offset:640
	ds_read_b128 v[50:53], v138 offset:704
	v_cvt_pk_bf16_f32 v147, v142, v143
	ds_bpermute_b32 v142, v139, v131
	v_pk_fma_f32 v[154:155], v[156:157], 2.0, 1.0 op_sel_hi:[1,0,0]
	v_permlane16_swap_b32_e32 v145, v147
	v_cvt_pk_bf16_f32 v146, v154, v155
	s_nop 1
	v_permlane16_swap_b32_e32 v144, v146
	global_store_dwordx4 v[164:165], v[144:147], off offset:128 nt
	s_and_saveexec_b64 s[2:3], s[0:1]
	s_cbranch_execz .LBB3_15
	s_waitcnt lgkmcnt(0)
	v_add_f32_e32 v144, v131, v142
	v_mov_b32_e32 v131, v195
	v_lshl_add_u64 v[142:143], v[130:131], 2, v[132:133]
	global_store_dword v[142:143], v144, off offset:64
.LBB3_15:
	s_or_b64 exec, exec, s[2:3]
	s_waitcnt lgkmcnt(0)
	v_exp_f32_e32 v142, v98
	v_exp_f32_e32 v144, v100
	v_exp_f32_e32 v145, v101
	v_exp_f32_e32 v143, v99
	v_exp_f32_e32 v156, v64
	v_exp_f32_e32 v157, v65
	v_pk_add_f32 v[144:145], v[144:145], 1.0 op_sel_hi:[1,0]
	v_pk_add_f32 v[148:149], v[142:143], 1.0 op_sel_hi:[1,0]
	v_rcp_f32_e64 v143, -v145
	v_rcp_f32_e64 v142, -v144
	v_rcp_f32_e64 v151, -v149
	v_rcp_f32_e64 v150, -v148
	v_pk_add_f32 v[156:157], v[156:157], 1.0 op_sel_hi:[1,0]
	v_pk_fma_f32 v[154:155], v[142:143], 2.0, 1.0 op_sel_hi:[1,0,0]
	v_rcp_f32_e64 v159, -v157
	v_pk_fma_f32 v[142:143], v[150:151], 2.0, 1.0 op_sel_hi:[1,0,0]
	v_exp_f32_e32 v150, v62
	v_exp_f32_e32 v151, v63
	v_rcp_f32_e64 v158, -v156
	v_cvt_pk_bf16_f32 v142, v142, v143
	v_cvt_pk_bf16_f32 v143, v154, v155
	v_pk_add_f32 v[150:151], v[150:151], 1.0 op_sel_hi:[1,0]
	v_pk_fma_f32 v[154:155], v[158:159], 2.0, 1.0 op_sel_hi:[1,0,0]
	v_rcp_f32_e64 v161, -v151
	v_rcp_f32_e64 v160, -v150
	v_pk_mul_f32 v[156:157], v[144:145], v[156:157]
	v_cvt_pk_bf16_f32 v145, v154, v155
	v_exp_f32_e32 v154, v94
	v_pk_fma_f32 v[158:159], v[160:161], 2.0, 1.0 op_sel_hi:[1,0,0]
	v_exp_f32_e32 v155, v95
	v_cvt_pk_bf16_f32 v144, v158, v159
	v_exp_f32_e32 v158, v96
	v_exp_f32_e32 v159, v97
	v_pk_mul_f32 v[148:149], v[148:149], v[150:151]
	v_pk_add_f32 v[154:155], v[154:155], 1.0 op_sel_hi:[1,0]
	v_pk_add_f32 v[100:101], v[100:101], 0 op_sel_hi:[1,0]
	v_pk_add_f32 v[158:159], v[158:159], 1.0 op_sel_hi:[1,0]
	v_rcp_f32_e64 v165, -v155
	v_rcp_f32_e64 v163, -v159
	v_rcp_f32_e64 v162, -v158
	v_rcp_f32_e64 v164, -v154
	v_pk_mul_f32 v[148:149], v[148:149], v[154:155]
	v_pk_mul_f32 v[154:155], v[156:157], v[158:159]
	v_exp_f32_e32 v156, v54
	v_exp_f32_e32 v158, v56
	v_exp_f32_e32 v159, v57
	v_exp_f32_e32 v157, v55
	v_pk_add_f32 v[98:99], v[98:99], 0 op_sel_hi:[1,0]
	v_pk_add_f32 v[150:151], v[100:101], v[64:65]
	v_bitop3_b32 v146, v141, s39, v224 bitop3:0xc8
	v_mov_b32_e32 v147, v195
	v_pk_add_f32 v[160:161], v[98:99], v[62:63]
	v_pk_add_f32 v[96:97], v[150:151], v[96:97]
	v_pk_add_f32 v[150:151], v[158:159], 1.0 op_sel_hi:[1,0]
	v_pk_add_f32 v[156:157], v[156:157], 1.0 op_sel_hi:[1,0]
	v_lshl_add_u64 v[146:147], v[200:201], 0, v[146:147]
	v_pk_add_f32 v[94:95], v[160:161], v[94:95]
	v_rcp_f32_e64 v159, -v151
	v_rcp_f32_e64 v158, -v150
	v_rcp_f32_e64 v161, -v157
	v_rcp_f32_e64 v160, -v156
	v_lshl_add_u64 v[152:153], v[146:147], 0, v[134:135]
	v_permlane16_swap_b32_e32 v142, v144
	v_permlane16_swap_b32_e32 v143, v145
	v_lshl_add_u64 v[152:153], v[152:153], 0, v[194:195]
	ds_read_b128 v[98:101], v138
	ds_read_b128 v[62:65], v138 offset:64
	global_store_dwordx4 v[152:153], v[142:145], off nt
	v_pk_fma_f32 v[158:159], v[158:159], 2.0, 1.0 op_sel_hi:[1,0,0]
	v_pk_mul_f32 v[148:149], v[148:149], v[156:157]
	v_pk_fma_f32 v[144:145], v[162:163], 2.0, 1.0 op_sel_hi:[1,0,0]
	v_pk_fma_f32 v[142:143], v[164:165], 2.0, 1.0 op_sel_hi:[1,0,0]
	v_pk_mul_f32 v[150:151], v[154:155], v[150:151]
	v_cvt_pk_bf16_f32 v142, v142, v143
	v_cvt_pk_bf16_f32 v143, v144, v145
	v_pk_fma_f32 v[144:145], v[160:161], 2.0, 1.0 op_sel_hi:[1,0,0]
	v_exp_f32_e32 v160, v84
	v_cvt_pk_bf16_f32 v144, v144, v145
	v_cvt_pk_bf16_f32 v145, v158, v159
	v_exp_f32_e32 v158, v82
	v_exp_f32_e32 v159, v83
	v_permlane16_swap_b32_e32 v142, v144
	v_exp_f32_e32 v161, v85
	v_permlane16_swap_b32_e32 v143, v145
	v_pk_add_f32 v[158:159], v[158:159], 1.0 op_sel_hi:[1,0]
	v_pk_add_f32 v[154:155], v[96:97], v[56:57]
	v_pk_add_f32 v[156:157], v[94:95], v[54:55]
	ds_read_b128 v[94:97], v138 offset:128
	ds_read_b128 v[54:57], v138 offset:192
	v_rcp_f32_e64 v165, -v159
	v_rcp_f32_e64 v164, -v158
	global_store_dwordx4 v[152:153], v[142:145], off offset:128 nt
	v_pk_mul_f32 v[148:149], v[148:149], v[158:159]
	v_exp_f32_e32 v152, v34
	v_exp_f32_e32 v158, v36
	v_exp_f32_e32 v159, v37
	v_exp_f32_e32 v153, v35
	v_pk_add_f32 v[160:161], v[160:161], 1.0 op_sel_hi:[1,0]
	v_pk_add_f32 v[84:85], v[154:155], v[84:85]
	v_rcp_f32_e64 v163, -v161
	v_rcp_f32_e64 v162, -v160
	v_pk_add_f32 v[154:155], v[158:159], 1.0 op_sel_hi:[1,0]
	v_pk_add_f32 v[152:153], v[152:153], 1.0 op_sel_hi:[1,0]
	v_pk_add_f32 v[82:83], v[156:157], v[82:83]
	v_rcp_f32_e64 v157, -v155
	v_rcp_f32_e64 v156, -v154
	v_rcp_f32_e64 v159, -v153
	v_rcp_f32_e64 v158, -v152
	v_pk_fma_f32 v[144:145], v[162:163], 2.0, 1.0 op_sel_hi:[1,0,0]
	v_pk_fma_f32 v[142:143], v[164:165], 2.0, 1.0 op_sel_hi:[1,0,0]
	v_pk_fma_f32 v[156:157], v[156:157], 2.0, 1.0 op_sel_hi:[1,0,0]
	v_cvt_pk_bf16_f32 v142, v142, v143
	v_cvt_pk_bf16_f32 v143, v144, v145
	v_pk_fma_f32 v[144:145], v[158:159], 2.0, 1.0 op_sel_hi:[1,0,0]
	v_exp_f32_e32 v158, v120
	v_cvt_pk_bf16_f32 v144, v144, v145
	v_cvt_pk_bf16_f32 v145, v156, v157
	v_exp_f32_e32 v156, v118
	v_exp_f32_e32 v159, v121
	v_exp_f32_e32 v157, v119
	v_pk_mul_f32 v[150:151], v[150:151], v[160:161]
	v_lshl_add_u64 v[146:147], v[146:147], 0, v[136:137]
	v_pk_mul_f32 v[150:151], v[150:151], v[154:155]
	v_pk_mul_f32 v[148:149], v[148:149], v[152:153]
	v_pk_add_f32 v[158:159], v[158:159], 1.0 op_sel_hi:[1,0]
	v_pk_add_f32 v[156:157], v[156:157], 1.0 op_sel_hi:[1,0]
	v_lshl_add_u64 v[164:165], v[146:147], 0, v[194:195]
	v_rcp_f32_e64 v163, -v157
	v_rcp_f32_e64 v162, -v156
	v_pk_mul_f32 v[146:147], v[148:149], v[156:157]
	v_pk_mul_f32 v[148:149], v[150:151], v[158:159]
	v_exp_f32_e32 v150, v46
	v_exp_f32_e32 v156, v48
	v_exp_f32_e32 v157, v49
	v_exp_f32_e32 v151, v47
	v_pk_add_f32 v[152:153], v[84:85], v[36:37]
	v_pk_add_f32 v[154:155], v[82:83], v[34:35]
	v_pk_add_f32 v[120:121], v[152:153], v[120:121]
	v_pk_add_f32 v[152:153], v[156:157], 1.0 op_sel_hi:[1,0]
	v_pk_add_f32 v[150:151], v[150:151], 1.0 op_sel_hi:[1,0]
	v_pk_mul_f32 v[148:149], v[148:149], v[152:153]
	v_pk_mul_f32 v[146:147], v[146:147], v[150:151]
	v_pk_add_f32 v[118:119], v[154:155], v[118:119]
	v_log_f32_e32 v131, v146
	v_log_f32_e32 v146, v147
	v_log_f32_e32 v147, v148
	v_log_f32_e32 v148, v149
	v_pk_add_f32 v[48:49], v[120:121], v[48:49]
	v_pk_add_f32 v[46:47], v[118:119], v[46:47]
	v_add_f32_e32 v118, v131, v146
	v_add_f32_e32 v119, v147, v148
	v_add_f32_e32 v46, v46, v47
	v_add_f32_e32 v47, v48, v49
	v_add_f32_e32 v118, v118, v119
	v_add_f32_e32 v46, v46, v47
	v_add_f32_e32 v118, 0xc2000000, v118
	v_mul_f32_e32 v131, 0xbeb17218, v46
	v_fmac_f32_e32 v131, 0x3f317218, v118
	v_rcp_f32_e64 v161, -v159
	v_rcp_f32_e64 v160, -v158
	ds_bpermute_b32 v148, v140, v131
	v_rcp_f32_e64 v155, -v153
	v_rcp_f32_e64 v154, -v152
	v_permlane16_swap_b32_e32 v142, v144
	v_permlane16_swap_b32_e32 v143, v145
	ds_read_b128 v[82:85], v138 offset:512
	ds_read_b128 v[34:37], v138 offset:576
	global_store_dwordx4 v[164:165], v[142:145], off nt
	v_rcp_f32_e64 v157, -v151
	v_rcp_f32_e64 v156, -v150
	v_pk_fma_f32 v[142:143], v[160:161], 2.0, 1.0 op_sel_hi:[1,0,0]
	v_pk_fma_f32 v[144:145], v[162:163], 2.0, 1.0 op_sel_hi:[1,0,0]
	s_waitcnt lgkmcnt(0)
	v_add_f32_e32 v131, v131, v148
	v_cvt_pk_bf16_f32 v144, v144, v145
	v_cvt_pk_bf16_f32 v145, v142, v143
	v_pk_fma_f32 v[142:143], v[154:155], 2.0, 1.0 op_sel_hi:[1,0,0]
	ds_read_b128 v[118:121], v138 offset:640
	ds_read_b128 v[46:49], v138 offset:704
	v_cvt_pk_bf16_f32 v147, v142, v143
	ds_bpermute_b32 v142, v139, v131
	v_pk_fma_f32 v[154:155], v[156:157], 2.0, 1.0 op_sel_hi:[1,0,0]
	v_permlane16_swap_b32_e32 v145, v147
	v_cvt_pk_bf16_f32 v146, v154, v155
	s_nop 1
	v_permlane16_swap_b32_e32 v144, v146
	global_store_dwordx4 v[164:165], v[144:147], off offset:128 nt
	s_and_saveexec_b64 s[2:3], s[0:1]
	s_cbranch_execz .LBB3_17
	s_waitcnt lgkmcnt(0)
	v_add_f32_e32 v144, v131, v142
	v_mov_b32_e32 v131, v195
	v_lshl_add_u64 v[142:143], v[130:131], 2, v[132:133]
	global_store_dword v[142:143], v144, off offset:512

.Lg1_noY:
	s_waitcnt lgkmcnt(0)
	v_exp_f32_e32 v142, v18
	v_exp_f32_e32 v144, v20
	v_exp_f32_e32 v145, v21
	v_exp_f32_e32 v143, v19
	v_exp_f32_e32 v154, v4
	v_exp_f32_e32 v155, v5
	v_pk_add_f32 v[144:145], v[144:145], 1.0 op_sel_hi:[1,0]
	v_pk_add_f32 v[148:149], v[142:143], 1.0 op_sel_hi:[1,0]
	v_rcp_f32_e64 v143, -v145
	v_rcp_f32_e64 v142, -v144
	v_rcp_f32_e64 v151, -v149
	v_rcp_f32_e64 v150, -v148
	v_pk_add_f32 v[154:155], v[154:155], 1.0 op_sel_hi:[1,0]
	v_pk_fma_f32 v[152:153], v[142:143], 2.0, 1.0 op_sel_hi:[1,0,0]
	v_rcp_f32_e64 v157, -v155
	v_pk_fma_f32 v[142:143], v[150:151], 2.0, 1.0 op_sel_hi:[1,0,0]
	v_exp_f32_e32 v150, v2
	v_exp_f32_e32 v151, v3
	v_rcp_f32_e64 v156, -v154
	v_cvt_pk_bf16_f32 v142, v142, v143
	v_cvt_pk_bf16_f32 v143, v152, v153
	v_pk_add_f32 v[150:151], v[150:151], 1.0 op_sel_hi:[1,0]
	v_pk_fma_f32 v[152:153], v[156:157], 2.0, 1.0 op_sel_hi:[1,0,0]
	v_rcp_f32_e64 v159, -v151
	v_rcp_f32_e64 v158, -v150
	v_pk_mul_f32 v[154:155], v[144:145], v[154:155]
	v_cvt_pk_bf16_f32 v145, v152, v153
	v_exp_f32_e32 v152, v26
	v_pk_fma_f32 v[156:157], v[158:159], 2.0, 1.0 op_sel_hi:[1,0,0]
	v_exp_f32_e32 v153, v27
	v_cvt_pk_bf16_f32 v144, v156, v157
	v_exp_f32_e32 v156, v28
	v_exp_f32_e32 v157, v29
	v_pk_mul_f32 v[148:149], v[148:149], v[150:151]
	v_pk_add_f32 v[152:153], v[152:153], 1.0 op_sel_hi:[1,0]
	v_pk_add_f32 v[20:21], v[20:21], 0 op_sel_hi:[1,0]
	v_pk_add_f32 v[156:157], v[156:157], 1.0 op_sel_hi:[1,0]
	v_rcp_f32_e64 v163, -v153
	v_rcp_f32_e64 v161, -v157
	v_rcp_f32_e64 v160, -v156
	v_rcp_f32_e64 v162, -v152
	v_pk_mul_f32 v[148:149], v[148:149], v[152:153]
	v_pk_mul_f32 v[152:153], v[154:155], v[156:157]
	v_exp_f32_e32 v154, v10
	v_exp_f32_e32 v156, v12
	v_exp_f32_e32 v157, v13
	v_exp_f32_e32 v155, v11
	v_pk_add_f32 v[18:19], v[18:19], 0 op_sel_hi:[1,0]
	v_pk_add_f32 v[150:151], v[20:21], v[4:5]
	v_bitop3_b32 v146, v141, s38, v225 bitop3:0xc8
	v_mov_b32_e32 v147, v195
	v_pk_add_f32 v[158:159], v[18:19], v[2:3]
	v_pk_add_f32 v[28:29], v[150:151], v[28:29]
	v_pk_add_f32 v[150:151], v[156:157], 1.0 op_sel_hi:[1,0]
	v_pk_add_f32 v[154:155], v[154:155], 1.0 op_sel_hi:[1,0]
	v_lshl_add_u64 v[146:147], v[200:201], 0, v[146:147]
	v_pk_add_f32 v[26:27], v[158:159], v[26:27]
	v_rcp_f32_e64 v157, -v151
	v_rcp_f32_e64 v156, -v150
	v_rcp_f32_e64 v159, -v155
	v_rcp_f32_e64 v158, -v154
	v_lshl_add_u64 v[134:135], v[146:147], 0, v[134:135]
	v_permlane16_swap_b32_e32 v142, v144
	v_permlane16_swap_b32_e32 v143, v145
	v_lshl_add_u64 v[134:135], v[134:135], 0, v[194:195]
	ds_read_b128 v[18:21], v138
	ds_read_b128 v[2:5], v138 offset:64
	global_store_dwordx4 v[134:135], v[142:145], off nt
	v_pk_fma_f32 v[156:157], v[156:157], 2.0, 1.0 op_sel_hi:[1,0,0]
	v_pk_mul_f32 v[150:151], v[152:153], v[150:151]
	v_pk_fma_f32 v[144:145], v[160:161], 2.0, 1.0 op_sel_hi:[1,0,0]
	v_pk_fma_f32 v[142:143], v[162:163], 2.0, 1.0 op_sel_hi:[1,0,0]
	v_pk_mul_f32 v[148:149], v[148:149], v[154:155]
	v_cvt_pk_bf16_f32 v142, v142, v143
	v_cvt_pk_bf16_f32 v143, v144, v145
	v_pk_fma_f32 v[144:145], v[158:159], 2.0, 1.0 op_sel_hi:[1,0,0]
	v_exp_f32_e32 v158, v24
	v_cvt_pk_bf16_f32 v144, v144, v145
	v_cvt_pk_bf16_f32 v145, v156, v157
	v_exp_f32_e32 v156, v22
	v_exp_f32_e32 v159, v25
	v_exp_f32_e32 v157, v23
	v_permlane16_swap_b32_e32 v142, v144
	v_permlane16_swap_b32_e32 v143, v145
	v_pk_add_f32 v[158:159], v[158:159], 1.0 op_sel_hi:[1,0]
	v_pk_add_f32 v[156:157], v[156:157], 1.0 op_sel_hi:[1,0]
	v_pk_add_f32 v[152:153], v[28:29], v[12:13]
	v_pk_add_f32 v[154:155], v[26:27], v[10:11]
	ds_read_b128 v[26:29], v138 offset:128
	ds_read_b128 v[10:13], v138 offset:192
	global_store_dwordx4 v[134:135], v[142:145], off offset:128 nt
	v_rcp_f32_e64 v161, -v159
	v_rcp_f32_e64 v160, -v158
	v_lshl_add_u64 v[142:143], v[146:147], 0, v[136:137]
	v_pk_mul_f32 v[144:145], v[148:149], v[156:157]
	v_pk_mul_f32 v[146:147], v[150:151], v[158:159]
	v_exp_f32_e32 v148, v6
	v_exp_f32_e32 v150, v8
	v_exp_f32_e32 v151, v9
	v_exp_f32_e32 v149, v7
	v_rcp_f32_e64 v163, -v157
	v_rcp_f32_e64 v162, -v156
	v_pk_add_f32 v[150:151], v[150:151], 1.0 op_sel_hi:[1,0]
	v_pk_add_f32 v[148:149], v[148:149], 1.0 op_sel_hi:[1,0]
	v_pk_add_f32 v[24:25], v[152:153], v[24:25]
	v_pk_add_f32 v[22:23], v[154:155], v[22:23]
	v_rcp_f32_e64 v153, -v151
	v_rcp_f32_e64 v152, -v150
	v_rcp_f32_e64 v155, -v149
	v_rcp_f32_e64 v154, -v148
	v_pk_fma_f32 v[136:137], v[160:161], 2.0, 1.0 op_sel_hi:[1,0,0]
	v_pk_fma_f32 v[134:135], v[162:163], 2.0, 1.0 op_sel_hi:[1,0,0]
	v_pk_fma_f32 v[152:153], v[152:153], 2.0, 1.0 op_sel_hi:[1,0,0]
	v_cvt_pk_bf16_f32 v134, v134, v135
	v_cvt_pk_bf16_f32 v135, v136, v137
	v_pk_fma_f32 v[136:137], v[154:155], 2.0, 1.0 op_sel_hi:[1,0,0]
	v_pk_mul_f32 v[144:145], v[144:145], v[148:149]
	v_cvt_pk_bf16_f32 v136, v136, v137
	v_cvt_pk_bf16_f32 v137, v152, v153
	v_exp_f32_e32 v152, v30
	v_exp_f32_e32 v153, v31
	v_exp_f32_e32 v154, v32
	v_exp_f32_e32 v155, v33
	v_lshl_add_u64 v[160:161], v[142:143], 0, v[194:195]
	v_pk_add_f32 v[152:153], v[152:153], 1.0 op_sel_hi:[1,0]
	v_exp_f32_e32 v142, v14
	v_rcp_f32_e64 v159, -v153
	v_rcp_f32_e64 v158, -v152
	v_pk_mul_f32 v[144:145], v[144:145], v[152:153]
	v_exp_f32_e32 v152, v16
	v_exp_f32_e32 v153, v17
	v_exp_f32_e32 v143, v15
	v_pk_mul_f32 v[146:147], v[146:147], v[150:151]
	v_pk_add_f32 v[148:149], v[24:25], v[8:9]
	v_pk_add_f32 v[150:151], v[22:23], v[6:7]
	v_pk_add_f32 v[154:155], v[154:155], 1.0 op_sel_hi:[1,0]
	v_pk_add_f32 v[32:33], v[148:149], v[32:33]
	v_pk_mul_f32 v[146:147], v[146:147], v[154:155]
	v_pk_add_f32 v[30:31], v[150:151], v[30:31]
	v_pk_add_f32 v[148:149], v[152:153], 1.0 op_sel_hi:[1,0]
	v_pk_add_f32 v[150:151], v[142:143], 1.0 op_sel_hi:[1,0]
	v_pk_mul_f32 v[146:147], v[146:147], v[148:149]
	v_pk_mul_f32 v[144:145], v[144:145], v[150:151]
	v_pk_add_f32 v[16:17], v[32:33], v[16:17]
	v_log_f32_e32 v131, v144
	v_log_f32_e32 v141, v145
	v_log_f32_e32 v144, v146
	v_log_f32_e32 v145, v147
	v_pk_add_f32 v[14:15], v[30:31], v[14:15]
	v_add_f32_e32 v30, v131, v141
	v_add_f32_e32 v14, v14, v15
	v_add_f32_e32 v31, v144, v145
	v_add_f32_e32 v15, v16, v17
	v_add_f32_e32 v30, v30, v31
	v_add_f32_e32 v14, v14, v15
	v_add_f32_e32 v30, 0xc2000000, v30
	v_mul_f32_e32 v131, 0xbeb17218, v14
	v_fmac_f32_e32 v131, 0x3f317218, v30
	v_rcp_f32_e64 v157, -v155
	v_rcp_f32_e64 v156, -v154
	ds_bpermute_b32 v140, v140, v131
	v_rcp_f32_e64 v153, -v149
	v_rcp_f32_e64 v152, -v148
	v_permlane16_swap_b32_e32 v134, v136
	v_permlane16_swap_b32_e32 v135, v137
	ds_read_b128 v[22:25], v138 offset:512
	ds_read_b128 v[6:9], v138 offset:576
	global_store_dwordx4 v[160:161], v[134:137], off nt
	v_rcp_f32_e64 v155, -v151
	v_rcp_f32_e64 v154, -v150
	v_pk_fma_f32 v[134:135], v[156:157], 2.0, 1.0 op_sel_hi:[1,0,0]
	s_waitcnt lgkmcnt(0)
	v_add_f32_e32 v131, v131, v140
	v_cvt_pk_bf16_f32 v143, v134, v135
	v_pk_fma_f32 v[134:135], v[152:153], 2.0, 1.0 op_sel_hi:[1,0,0]
	ds_read_b128 v[30:33], v138 offset:640
	ds_read_b128 v[14:17], v138 offset:704
	v_cvt_pk_bf16_f32 v145, v134, v135
	ds_bpermute_b32 v134, v139, v131
	v_pk_fma_f32 v[136:137], v[158:159], 2.0, 1.0 op_sel_hi:[1,0,0]
	v_permlane16_swap_b32_e32 v143, v145
	v_cvt_pk_bf16_f32 v142, v136, v137
	v_pk_fma_f32 v[136:137], v[154:155], 2.0, 1.0 op_sel_hi:[1,0,0]
	s_nop 0
	v_cvt_pk_bf16_f32 v144, v136, v137
	s_nop 1
	v_permlane16_swap_b32_e32 v142, v144
	global_store_dwordx4 v[160:161], v[142:145], off offset:128 nt
	s_and_saveexec_b64 s[2:3], s[0:1]
	s_cbranch_execz .LBB3_5
	s_waitcnt lgkmcnt(0)
	v_add_f32_e32 v134, v131, v134
	v_mov_b32_e32 v131, v195
	v_lshl_add_u64 v[130:131], v[130:131], 2, v[132:133]
	global_store_dword v[130:131], v134, off offset:576
	s_branch .LBB3_5
